# transpose phase: tile load software-pipelined one unit ahead (counted vmcnt(1) leaves the previous tile store in flight)
# speedup vs baseline: 1.0155x; 1.0026x over previous
.LBB0_1139:
	s_ashr_i32 s11, s7, 31
	s_lshr_b32 s11, s11, 28
	s_add_i32 s11, s7, s11
	s_ashr_i32 s11, s11, 4
	s_lshl_b32 s13, s11, 10
	s_sub_i32 s14, s8, s13
	v_add_u32_e32 v24, s14, v1
	v_ashrrev_i32_e32 v25, 31, v24
	s_lshl_b32 s12, s11, 6
	v_lshlrev_b64 v[24:25], 15, v[24:25]
	s_ashr_i32 s13, s12, 31
	v_lshl_add_u64 v[24:25], s[0:1], 0, v[24:25]
	v_lshl_add_u64 v[24:25], s[12:13], 1, v[24:25]
	v_lshl_add_u64 v[24:25], v[24:25], 0, v[2:3]
	global_load_dwordx4 v[20:23], v[24:25], off
	s_waitcnt vmcnt(0)
	s_branch .Lc2_body_L0
.Lc2_top_L0:
	s_waitcnt vmcnt(1)
.Lc2_body_L0:
	v_add_u32_e32 v12, s12, v1
	s_barrier
	v_ashrrev_i32_e32 v13, 31, v12
	v_lshlrev_b64 v[12:13], 11, v[12:13]
	s_ashr_i32 s15, s14, 31
	v_lshl_add_u64 v[12:13], s[4:5], 0, v[12:13]
	s_add_i32 s7, s7, s6
	s_add_i32 s8, s8, s9
	v_lshl_add_u64 v[12:13], s[14:15], 1, v[12:13]
	v_lshl_add_u64 v[12:13], v[12:13], 0, v[2:3]
	ds_write_b128 v4, v[20:23]
	s_waitcnt lgkmcnt(0)
	s_cmpk_lt_i32 s7, 0x1000
	s_cbranch_scc0 .Lc2_nopf_L0
	s_ashr_i32 s11, s7, 31
	s_lshr_b32 s11, s11, 28
	s_add_i32 s11, s7, s11
	s_ashr_i32 s11, s11, 4
	s_lshl_b32 s13, s11, 10
	s_sub_i32 s14, s8, s13
	v_add_u32_e32 v24, s14, v1
	v_ashrrev_i32_e32 v25, 31, v24
	s_lshl_b32 s12, s11, 6
	v_lshlrev_b64 v[24:25], 15, v[24:25]
	s_ashr_i32 s13, s12, 31
	v_lshl_add_u64 v[24:25], s[0:1], 0, v[24:25]
	v_lshl_add_u64 v[24:25], s[12:13], 1, v[24:25]
	v_lshl_add_u64 v[24:25], v[24:25], 0, v[2:3]
	global_load_dwordx4 v[20:23], v[24:25], off
.Lc2_nopf_L0:
	s_barrier
	ds_read_u16 v7, v6 offset:288
	ds_read_u16 v8, v6 offset:432
	ds_read_u16 v9, v6 offset:576
	ds_read_u16 v10, v6 offset:864
	ds_read_u16 v11, v6 offset:1008
	ds_read_u16 v14, v6 offset:720
	ds_read_u16 v15, v5
	ds_read_u16 v16, v6 offset:144
	s_waitcnt lgkmcnt(3)
	v_perm_b32 v11, v11, v10, s10
	s_waitcnt lgkmcnt(2)
	v_perm_b32 v10, v14, v9, s10
	v_perm_b32 v9, v8, v7, s10
	s_waitcnt lgkmcnt(0)
	v_perm_b32 v8, v16, v15, s10
	global_store_dwordx4 v[12:13], v[8:11], off
	s_cmpk_lt_i32 s7, 0x1000
	s_cbranch_scc1 .Lc2_top_L0

.LBB0_3171:
	s_ashr_i32 s11, s6, 31
	s_lshr_b32 s11, s11, 28
	s_add_i32 s11, s6, s11
	s_ashr_i32 s11, s11, 4
	s_lshl_b32 s13, s11, 10
	s_sub_i32 s14, s8, s13
	v_add_u32_e32 v24, s14, v1
	v_ashrrev_i32_e32 v25, 31, v24
	s_lshl_b32 s12, s11, 6
	v_lshlrev_b64 v[24:25], 15, v[24:25]
	s_ashr_i32 s13, s12, 31
	v_lshl_add_u64 v[24:25], s[0:1], 0, v[24:25]
	v_lshl_add_u64 v[24:25], s[12:13], 1, v[24:25]
	v_lshl_add_u64 v[24:25], v[24:25], 0, v[2:3]
	global_load_dwordx4 v[20:23], v[24:25], off
	s_waitcnt vmcnt(0)
	s_branch .Lc2_body_L1

.Lc2_body_L1:
	v_add_u32_e32 v12, s12, v1
	s_barrier
	v_ashrrev_i32_e32 v13, 31, v12
	v_lshlrev_b64 v[12:13], 11, v[12:13]
	s_ashr_i32 s15, s14, 31
	v_lshl_add_u64 v[12:13], s[4:5], 0, v[12:13]
	s_add_i32 s6, s6, s7
	s_add_i32 s8, s8, s9
	v_lshl_add_u64 v[12:13], s[14:15], 1, v[12:13]
	v_lshl_add_u64 v[12:13], v[12:13], 0, v[2:3]
	ds_write_b128 v4, v[20:23]
	s_waitcnt lgkmcnt(0)
	s_cmpk_lt_i32 s6, 0x1000
	s_cbranch_scc0 .Lc2_nopf_L1
	s_ashr_i32 s11, s6, 31
	s_lshr_b32 s11, s11, 28
	s_add_i32 s11, s6, s11
	s_ashr_i32 s11, s11, 4
	s_lshl_b32 s13, s11, 10
	s_sub_i32 s14, s8, s13
	v_add_u32_e32 v24, s14, v1
	v_ashrrev_i32_e32 v25, 31, v24
	s_lshl_b32 s12, s11, 6
	v_lshlrev_b64 v[24:25], 15, v[24:25]
	s_ashr_i32 s13, s12, 31
	v_lshl_add_u64 v[24:25], s[0:1], 0, v[24:25]
	v_lshl_add_u64 v[24:25], s[12:13], 1, v[24:25]
	v_lshl_add_u64 v[24:25], v[24:25], 0, v[2:3]
	global_load_dwordx4 v[20:23], v[24:25], off
.Lc2_nopf_L1:
	s_barrier
	ds_read_u16 v7, v6 offset:288
	ds_read_u16 v8, v6 offset:432
	ds_read_u16 v9, v6 offset:576
	ds_read_u16 v10, v6 offset:864
	ds_read_u16 v11, v6 offset:1008
	ds_read_u16 v14, v6 offset:720
	ds_read_u16 v15, v5
	ds_read_u16 v16, v6 offset:144
	s_waitcnt lgkmcnt(3)
	v_perm_b32 v11, v11, v10, s10
	s_waitcnt lgkmcnt(2)
	v_perm_b32 v10, v14, v9, s10
	v_perm_b32 v9, v8, v7, s10
	s_waitcnt lgkmcnt(0)
	v_perm_b32 v8, v16, v15, s10
	global_store_dwordx4 v[12:13], v[8:11], off
	s_cmpk_lt_i32 s6, 0x1000
	s_cbranch_scc1 .Lc2_top_L1
